# speedup vs baseline: 1.0131x; 1.0028x over previous
.LBB0_21:
	v_exp_f32_e64 v156, -|v154|
	v_max_f32 v157, 0, v154
	v_add_f32 v156, 1.0, v156
	v_log_f32 v156, v156
	s_nop 0
	v_fma_mixlo_f16 v155, v156, 1.0, v157
	ds_write_b16 v148, v155
	v_mov_b32_e32 v192, v106
	v_mov_b32_e32 v193, v110
	v_mul_f32 v182, -2.0, v153
	s_nop 6
	ds_read_b128 v[208:211], v139
	s_waitcnt lgkmcnt(1)
	s_barrier
	ds_read_b128 v[212:215], v140
	ds_read_b128 v[216:219], v141
	s_waitcnt lgkmcnt(2)
	v_smfmac_f32_16x16x64_f16 v[192:195], v[208:211], v[6:13], v191
	ds_read_b128 v[220:223], v142
	s_waitcnt lgkmcnt(2)
	v_smfmac_f32_16x16x64_f16 v[192:195], v[212:215], v[14:21], v191
	s_waitcnt lgkmcnt(1)
	v_smfmac_f32_16x16x64_f16 v[192:195], v[216:219], v[26:33], v191
	s_waitcnt lgkmcnt(0)
	v_smfmac_f32_16x16x64_f16 v[192:195], v[220:223], v[34:41], v191
	s_nop 7
	v_cndmask_b32_e64 v154, v192, v193, s[0:1]
	v_exp_f32_e64 v156, -|v154|
	v_max_f32 v157, 0, v154
	v_add_f32 v156, 1.0, v156
	v_log_f32 v156, v156
	s_nop 0
	v_fma_mixlo_f16 v155, v156, 1.0, v157
	ds_write_b16 v149, v155
	v_mov_b32_e32 v200, v114
	v_mov_b32_e32 v201, v118
	v_mov_b32_e32 v204, v122
	v_mov_b32_e32 v205, v126
	s_nop 3
	ds_read_b128 v[208:211], v143
	s_waitcnt lgkmcnt(1)
	s_barrier
	ds_read_b128 v[212:215], v144
	ds_read_b128 v[216:219], v145
	s_waitcnt lgkmcnt(2)
	v_smfmac_f32_16x16x64_f16 v[200:203], v[208:211], v[42:49], v191
	ds_read_b128 v[220:223], v146
	v_smfmac_f32_16x16x64_f16 v[204:207], v[208:211], v[74:81], v191
	s_waitcnt lgkmcnt(2)
	v_smfmac_f32_16x16x64_f16 v[200:203], v[212:215], v[50:57], v191
	v_smfmac_f32_16x16x64_f16 v[204:207], v[212:215], v[82:89], v191
	s_waitcnt lgkmcnt(1)
	v_smfmac_f32_16x16x64_f16 v[200:203], v[216:219], v[58:65], v191
	v_smfmac_f32_16x16x64_f16 v[204:207], v[216:219], v[90:97], v191
	s_waitcnt lgkmcnt(0)
	v_smfmac_f32_16x16x64_f16 v[200:203], v[220:223], v[66:73], v191
	v_smfmac_f32_16x16x64_f16 v[204:207], v[220:223], v[98:105], v191
	s_nop 6
	v_cndmask_b32_e64 v170, v201, v200, s[6:7]
	v_cndmask_b32_e64 v170, v170, v204, s[0:1]
	v_cndmask_b32_e64 v170, v170, v205, s[4:5]
	v_exp_f32_e32 v170, v170
	s_nop 0
	v_add_f32_e32 v170, 1.0, v170
	v_rcp_f32_e32 v170, v170
	s_nop 0
	v_fmac_f32_e32 v153, v170, v182
	s_nop 1
	v_add_f32_dpp v153, v153, v153 quad_perm:[1,0,3,2] row_mask:0xf bank_mask:0xf bound_ctrl:1
	s_nop 1
	v_add_f32_dpp v153, v153, v153 quad_perm:[2,3,0,1] row_mask:0xf bank_mask:0xf bound_ctrl:1
	s_nop 1
	v_add_f32_dpp v153, v153, v153 row_half_mirror row_mask:0xf bank_mask:0xf bound_ctrl:1
	v_cvt_f16_f32_e32 v170, v153
	ds_write_b16 v150, v170
	s_waitcnt lgkmcnt(0)
	s_barrier
	ds_read_b128 v[154:157], v147
	s_waitcnt lgkmcnt(0)
	v_smfmac_f32_16x16x64_f16 v[130:133], v[154:157], v[248:255], v191
	s_nop 2
	v_add_u32_e32 v134, s3, v151
	ds_read_b32 v135, v134
	s_nop 2
	v_cndmask_b32_e64 v136, v130, v131, s[0:1]
	v_exp_f32_e64 v158, -|v136|
	v_max_f32 v159, 0, v136
	v_add_f32 v158, 1.0, v158
	v_log_f32 v158, v158
	s_nop 0
	v_fma_mixlo_f16 v137, v158, 1.0, v159
	ds_write_b16 v148, v137
	v_mov_b32_e32 v192, v106
	v_mov_b32_e32 v193, v110
	v_add_f32_e32 v136, v152, v153
	v_mul_f32 v137, -2.0, v135
	s_nop 6
	ds_read_b128 v[208:211], v139
	s_waitcnt lgkmcnt(1)
	s_barrier
	ds_read_b128 v[212:215], v140
	ds_read_b128 v[216:219], v141
	s_waitcnt lgkmcnt(2)
	v_smfmac_f32_16x16x64_f16 v[192:195], v[208:211], v[6:13], v191
	ds_read_b128 v[220:223], v142
	s_waitcnt lgkmcnt(2)
	v_smfmac_f32_16x16x64_f16 v[192:195], v[212:215], v[14:21], v191
	s_waitcnt lgkmcnt(1)
	v_smfmac_f32_16x16x64_f16 v[192:195], v[216:219], v[26:33], v191
	s_waitcnt lgkmcnt(0)
	v_smfmac_f32_16x16x64_f16 v[192:195], v[220:223], v[34:41], v191
	s_nop 7
	v_cndmask_b32_e64 v152, v192, v193, s[0:1]
	v_exp_f32_e64 v158, -|v152|
	v_max_f32 v159, 0, v152
	v_add_f32 v158, 1.0, v158
	v_log_f32 v158, v158
	s_nop 0
	v_fma_mixlo_f16 v153, v158, 1.0, v159
	ds_write_b16 v149, v153
	v_mov_b32_e32 v200, v114
	v_mov_b32_e32 v201, v118
	v_mov_b32_e32 v204, v122
	v_mov_b32_e32 v205, v126
	s_nop 3
	ds_read_b128 v[208:211], v143
	s_waitcnt lgkmcnt(1)
	s_barrier
	ds_read_b128 v[212:215], v144
	ds_read_b128 v[216:219], v145
	s_waitcnt lgkmcnt(2)
	v_smfmac_f32_16x16x64_f16 v[200:203], v[208:211], v[42:49], v191
	ds_read_b128 v[220:223], v146
	v_smfmac_f32_16x16x64_f16 v[204:207], v[208:211], v[74:81], v191
	s_waitcnt lgkmcnt(2)
	v_smfmac_f32_16x16x64_f16 v[200:203], v[212:215], v[50:57], v191
	v_smfmac_f32_16x16x64_f16 v[204:207], v[212:215], v[82:89], v191
	s_waitcnt lgkmcnt(1)
	v_smfmac_f32_16x16x64_f16 v[200:203], v[216:219], v[58:65], v191
	v_smfmac_f32_16x16x64_f16 v[204:207], v[216:219], v[90:97], v191
	s_waitcnt lgkmcnt(0)
	v_smfmac_f32_16x16x64_f16 v[200:203], v[220:223], v[66:73], v191
	v_smfmac_f32_16x16x64_f16 v[204:207], v[220:223], v[98:105], v191
	s_nop 6
	v_cndmask_b32_e64 v152, v201, v200, s[6:7]
	v_cndmask_b32_e64 v152, v152, v204, s[0:1]
	v_cndmask_b32_e64 v152, v152, v205, s[4:5]
	v_exp_f32_e32 v152, v152
	s_nop 0
	v_add_f32_e32 v152, 1.0, v152
	v_rcp_f32_e32 v152, v152
	s_nop 0
	v_fmac_f32_e32 v135, v152, v137
	s_nop 1
	v_add_f32_dpp v135, v135, v135 quad_perm:[1,0,3,2] row_mask:0xf bank_mask:0xf bound_ctrl:1
	s_nop 1
	v_add_f32_dpp v135, v135, v135 quad_perm:[2,3,0,1] row_mask:0xf bank_mask:0xf bound_ctrl:1
	s_nop 1
	v_add_f32_dpp v135, v135, v135 row_half_mirror row_mask:0xf bank_mask:0xf bound_ctrl:1
	v_cvt_f16_f32_e32 v137, v135
	ds_write_b16 v150, v137
	s_waitcnt lgkmcnt(0)
	s_barrier
	ds_read_b128 v[158:161], v147
	s_nop 3
	ds_read_b32 v137, v134 offset:32
	v_add_f32_e32 v135, v136, v135
	s_waitcnt lgkmcnt(1)
	v_smfmac_f32_16x16x64_f16 v[130:133], v[158:161], v[248:255], v191
	s_nop 7
	v_cndmask_b32_e64 v156, v130, v131, s[0:1]
	v_exp_f32_e64 v158, -|v156|
	v_max_f32 v159, 0, v156
	v_add_f32 v158, 1.0, v158
	v_log_f32 v158, v158
	s_nop 0
	v_fma_mixlo_f16 v157, v158, 1.0, v159
	ds_write_b16 v148, v157
	v_mov_b32_e32 v192, v106
	v_mov_b32_e32 v193, v110
	v_mul_f32 v136, -2.0, v137
	s_nop 6
	ds_read_b128 v[208:211], v139
	s_waitcnt lgkmcnt(1)
	s_barrier
	ds_read_b128 v[212:215], v140
	ds_read_b128 v[216:219], v141
	s_waitcnt lgkmcnt(2)
	v_smfmac_f32_16x16x64_f16 v[192:195], v[208:211], v[6:13], v191
	ds_read_b128 v[220:223], v142
	s_waitcnt lgkmcnt(2)
	v_smfmac_f32_16x16x64_f16 v[192:195], v[212:215], v[14:21], v191
	s_waitcnt lgkmcnt(1)
	v_smfmac_f32_16x16x64_f16 v[192:195], v[216:219], v[26:33], v191
	s_waitcnt lgkmcnt(0)
	v_smfmac_f32_16x16x64_f16 v[192:195], v[220:223], v[34:41], v191
	s_nop 7
	v_cndmask_b32_e64 v156, v192, v193, s[0:1]
	v_exp_f32_e64 v158, -|v156|
	v_max_f32 v159, 0, v156
	v_add_f32 v158, 1.0, v158
	v_log_f32 v158, v158
	s_nop 0
	v_fma_mixlo_f16 v157, v158, 1.0, v159
	ds_write_b16 v149, v157
	v_mov_b32_e32 v200, v114
	v_mov_b32_e32 v201, v118
	v_mov_b32_e32 v204, v122
	v_mov_b32_e32 v205, v126
	s_nop 3
	ds_read_b128 v[208:211], v143
	s_waitcnt lgkmcnt(1)
	s_barrier
	ds_read_b128 v[212:215], v144
	ds_read_b128 v[216:219], v145
	s_waitcnt lgkmcnt(2)
	v_smfmac_f32_16x16x64_f16 v[200:203], v[208:211], v[42:49], v191
	ds_read_b128 v[220:223], v146
	v_smfmac_f32_16x16x64_f16 v[204:207], v[208:211], v[74:81], v191
	s_waitcnt lgkmcnt(2)
	v_smfmac_f32_16x16x64_f16 v[200:203], v[212:215], v[50:57], v191
	v_smfmac_f32_16x16x64_f16 v[204:207], v[212:215], v[82:89], v191
	s_waitcnt lgkmcnt(1)
	v_smfmac_f32_16x16x64_f16 v[200:203], v[216:219], v[58:65], v191
	v_smfmac_f32_16x16x64_f16 v[204:207], v[216:219], v[90:97], v191
	s_waitcnt lgkmcnt(0)
	v_smfmac_f32_16x16x64_f16 v[200:203], v[220:223], v[66:73], v191
	v_smfmac_f32_16x16x64_f16 v[204:207], v[220:223], v[98:105], v191
	s_nop 6
	v_cndmask_b32_e64 v172, v201, v200, s[6:7]
	v_cndmask_b32_e64 v172, v172, v204, s[0:1]
	v_cndmask_b32_e64 v172, v172, v205, s[4:5]
	v_exp_f32_e32 v172, v172
	s_nop 0
	v_add_f32_e32 v172, 1.0, v172
	v_rcp_f32_e32 v172, v172
	s_nop 0
	v_fmac_f32_e32 v137, v172, v136
	s_nop 1
	v_add_f32_dpp v136, v137, v137 quad_perm:[1,0,3,2] row_mask:0xf bank_mask:0xf bound_ctrl:1
	s_nop 1
	v_add_f32_dpp v136, v136, v136 quad_perm:[2,3,0,1] row_mask:0xf bank_mask:0xf bound_ctrl:1
	s_nop 1
	v_add_f32_dpp v136, v136, v136 row_half_mirror row_mask:0xf bank_mask:0xf bound_ctrl:1
	v_cvt_f16_f32_e32 v137, v136
	ds_write_b16 v150, v137
	s_waitcnt lgkmcnt(0)
	s_barrier
	ds_read_b128 v[156:159], v147
	s_nop 3
	ds_read_b32 v137, v134 offset:64
	v_add_f32_e32 v135, v135, v136
	s_waitcnt lgkmcnt(1)
	v_smfmac_f32_16x16x64_f16 v[130:133], v[156:159], v[248:255], v191
	s_nop 7
	v_cndmask_b32_e64 v156, v130, v131, s[0:1]
	v_exp_f32_e64 v158, -|v156|
	v_max_f32 v159, 0, v156
	v_add_f32 v158, 1.0, v158
	v_log_f32 v158, v158
	s_nop 0
	v_fma_mixlo_f16 v157, v158, 1.0, v159
	ds_write_b16 v148, v157
	v_mov_b32_e32 v192, v106
	v_mov_b32_e32 v193, v110
	v_mul_f32 v136, -2.0, v137
	s_nop 6
	ds_read_b128 v[208:211], v139
	s_waitcnt lgkmcnt(1)
	s_barrier
	ds_read_b128 v[212:215], v140
	ds_read_b128 v[216:219], v141
	s_waitcnt lgkmcnt(2)
	v_smfmac_f32_16x16x64_f16 v[192:195], v[208:211], v[6:13], v191
	ds_read_b128 v[220:223], v142
	s_waitcnt lgkmcnt(2)
	v_smfmac_f32_16x16x64_f16 v[192:195], v[212:215], v[14:21], v191
	s_waitcnt lgkmcnt(1)
	v_smfmac_f32_16x16x64_f16 v[192:195], v[216:219], v[26:33], v191
	s_waitcnt lgkmcnt(0)
	v_smfmac_f32_16x16x64_f16 v[192:195], v[220:223], v[34:41], v191
	s_nop 7
	v_cndmask_b32_e64 v156, v192, v193, s[0:1]
	v_exp_f32_e64 v158, -|v156|
	v_max_f32 v159, 0, v156
	v_add_f32 v158, 1.0, v158
	v_log_f32 v158, v158
	s_nop 0
	v_fma_mixlo_f16 v157, v158, 1.0, v159
	ds_write_b16 v149, v157
	v_mov_b32_e32 v200, v114
	v_mov_b32_e32 v201, v118
	v_mov_b32_e32 v204, v122
	v_mov_b32_e32 v205, v126
	s_nop 3
	ds_read_b128 v[208:211], v143
	s_waitcnt lgkmcnt(1)
	s_barrier
	ds_read_b128 v[212:215], v144
	ds_read_b128 v[216:219], v145
	s_waitcnt lgkmcnt(2)
	v_smfmac_f32_16x16x64_f16 v[200:203], v[208:211], v[42:49], v191
	ds_read_b128 v[220:223], v146
	v_smfmac_f32_16x16x64_f16 v[204:207], v[208:211], v[74:81], v191
	s_waitcnt lgkmcnt(2)
	v_smfmac_f32_16x16x64_f16 v[200:203], v[212:215], v[50:57], v191
	v_smfmac_f32_16x16x64_f16 v[204:207], v[212:215], v[82:89], v191
	s_waitcnt lgkmcnt(1)
	v_smfmac_f32_16x16x64_f16 v[200:203], v[216:219], v[58:65], v191
	v_smfmac_f32_16x16x64_f16 v[204:207], v[216:219], v[90:97], v191
	s_waitcnt lgkmcnt(0)
	v_smfmac_f32_16x16x64_f16 v[200:203], v[220:223], v[66:73], v191
	v_smfmac_f32_16x16x64_f16 v[204:207], v[220:223], v[98:105], v191
	s_nop 6
	v_cndmask_b32_e64 v172, v201, v200, s[6:7]
	v_cndmask_b32_e64 v172, v172, v204, s[0:1]
	v_cndmask_b32_e64 v172, v172, v205, s[4:5]
	v_exp_f32_e32 v172, v172
	s_nop 0
	v_add_f32_e32 v172, 1.0, v172
	v_rcp_f32_e32 v172, v172
	s_nop 0
	v_fmac_f32_e32 v137, v172, v136
	s_nop 1
	v_add_f32_dpp v136, v137, v137 quad_perm:[1,0,3,2] row_mask:0xf bank_mask:0xf bound_ctrl:1
	s_nop 1
	v_add_f32_dpp v136, v136, v136 quad_perm:[2,3,0,1] row_mask:0xf bank_mask:0xf bound_ctrl:1
	s_nop 1
	v_add_f32_dpp v136, v136, v136 row_half_mirror row_mask:0xf bank_mask:0xf bound_ctrl:1
	v_cvt_f16_f32_e32 v137, v136
	ds_write_b16 v150, v137
	s_waitcnt lgkmcnt(0)
	s_barrier
	ds_read_b128 v[156:159], v147
	s_nop 3
	ds_read_b32 v137, v134 offset:96
	v_add_f32_e32 v135, v135, v136
	s_waitcnt lgkmcnt(1)
	v_smfmac_f32_16x16x64_f16 v[130:133], v[156:159], v[248:255], v191
	s_nop 7
	v_cndmask_b32_e64 v156, v130, v131, s[0:1]
	v_exp_f32_e64 v158, -|v156|
	v_max_f32 v159, 0, v156
	v_add_f32 v158, 1.0, v158
	v_log_f32 v158, v158
	s_nop 0
	v_fma_mixlo_f16 v157, v158, 1.0, v159
	ds_write_b16 v148, v157
	v_mov_b32_e32 v192, v106
	v_mov_b32_e32 v193, v110
	v_mul_f32 v136, -2.0, v137
	s_nop 6
	ds_read_b128 v[208:211], v139
	s_waitcnt lgkmcnt(1)
	s_barrier
	ds_read_b128 v[212:215], v140
	ds_read_b128 v[216:219], v141
	s_waitcnt lgkmcnt(2)
	v_smfmac_f32_16x16x64_f16 v[192:195], v[208:211], v[6:13], v191
	ds_read_b128 v[220:223], v142
	s_waitcnt lgkmcnt(2)
	v_smfmac_f32_16x16x64_f16 v[192:195], v[212:215], v[14:21], v191
	s_waitcnt lgkmcnt(1)
	v_smfmac_f32_16x16x64_f16 v[192:195], v[216:219], v[26:33], v191
	s_waitcnt lgkmcnt(0)
	v_smfmac_f32_16x16x64_f16 v[192:195], v[220:223], v[34:41], v191
	s_nop 7
	v_cndmask_b32_e64 v156, v192, v193, s[0:1]
	v_exp_f32_e64 v158, -|v156|
	v_max_f32 v159, 0, v156
	v_add_f32 v158, 1.0, v158
	v_log_f32 v158, v158
	s_nop 0
	v_fma_mixlo_f16 v157, v158, 1.0, v159
	ds_write_b16 v149, v157
	v_mov_b32_e32 v200, v114
	v_mov_b32_e32 v201, v118
	v_mov_b32_e32 v204, v122
	v_mov_b32_e32 v205, v126
	s_nop 3
	ds_read_b128 v[208:211], v143
	s_waitcnt lgkmcnt(1)
	s_barrier
	ds_read_b128 v[212:215], v144
	ds_read_b128 v[216:219], v145
	s_waitcnt lgkmcnt(2)
	v_smfmac_f32_16x16x64_f16 v[200:203], v[208:211], v[42:49], v191
	ds_read_b128 v[220:223], v146
	v_smfmac_f32_16x16x64_f16 v[204:207], v[208:211], v[74:81], v191
	s_waitcnt lgkmcnt(2)
	v_smfmac_f32_16x16x64_f16 v[200:203], v[212:215], v[50:57], v191
	v_smfmac_f32_16x16x64_f16 v[204:207], v[212:215], v[82:89], v191
	s_waitcnt lgkmcnt(1)
	v_smfmac_f32_16x16x64_f16 v[200:203], v[216:219], v[58:65], v191
	v_smfmac_f32_16x16x64_f16 v[204:207], v[216:219], v[90:97], v191
	s_waitcnt lgkmcnt(0)
	v_smfmac_f32_16x16x64_f16 v[200:203], v[220:223], v[66:73], v191
	v_smfmac_f32_16x16x64_f16 v[204:207], v[220:223], v[98:105], v191
	s_nop 6
	v_cndmask_b32_e64 v172, v201, v200, s[6:7]
	v_cndmask_b32_e64 v172, v172, v204, s[0:1]
	v_cndmask_b32_e64 v172, v172, v205, s[4:5]
	v_exp_f32_e32 v172, v172
	s_nop 0
	v_add_f32_e32 v172, 1.0, v172
	v_rcp_f32_e32 v172, v172
	s_nop 0
	v_fmac_f32_e32 v137, v172, v136
	s_nop 1
	v_add_f32_dpp v136, v137, v137 quad_perm:[1,0,3,2] row_mask:0xf bank_mask:0xf bound_ctrl:1
	s_nop 1
	v_add_f32_dpp v136, v136, v136 quad_perm:[2,3,0,1] row_mask:0xf bank_mask:0xf bound_ctrl:1
	s_nop 1
	v_add_f32_dpp v136, v136, v136 row_half_mirror row_mask:0xf bank_mask:0xf bound_ctrl:1
	v_cvt_f16_f32_e32 v137, v136
	ds_write_b16 v150, v137
	s_waitcnt lgkmcnt(0)
	s_barrier
	ds_read_b128 v[156:159], v147
	s_nop 3
	ds_read_b32 v137, v134 offset:128
	v_add_f32_e32 v135, v135, v136
	s_waitcnt lgkmcnt(1)
	v_smfmac_f32_16x16x64_f16 v[130:133], v[156:159], v[248:255], v191
	s_nop 7
	v_cndmask_b32_e64 v156, v130, v131, s[0:1]
	v_exp_f32_e64 v158, -|v156|
	v_max_f32 v159, 0, v156
	v_add_f32 v158, 1.0, v158
	v_log_f32 v158, v158
	s_nop 0
	v_fma_mixlo_f16 v157, v158, 1.0, v159
	ds_write_b16 v148, v157
	v_mov_b32_e32 v192, v106
	v_mov_b32_e32 v193, v110
	v_mul_f32 v136, -2.0, v137
	s_nop 6
	ds_read_b128 v[208:211], v139
	s_waitcnt lgkmcnt(1)
	s_barrier
	ds_read_b128 v[212:215], v140
	ds_read_b128 v[216:219], v141
	s_waitcnt lgkmcnt(2)
	v_smfmac_f32_16x16x64_f16 v[192:195], v[208:211], v[6:13], v191
	ds_read_b128 v[220:223], v142
	s_waitcnt lgkmcnt(2)
	v_smfmac_f32_16x16x64_f16 v[192:195], v[212:215], v[14:21], v191
	s_waitcnt lgkmcnt(1)
	v_smfmac_f32_16x16x64_f16 v[192:195], v[216:219], v[26:33], v191
	s_waitcnt lgkmcnt(0)
	v_smfmac_f32_16x16x64_f16 v[192:195], v[220:223], v[34:41], v191
	s_nop 7
	v_cndmask_b32_e64 v156, v192, v193, s[0:1]
	v_exp_f32_e64 v158, -|v156|
	v_max_f32 v159, 0, v156
	v_add_f32 v158, 1.0, v158
	v_log_f32 v158, v158
	s_nop 0
	v_fma_mixlo_f16 v157, v158, 1.0, v159
	ds_write_b16 v149, v157
	v_mov_b32_e32 v200, v114
	v_mov_b32_e32 v201, v118
	v_mov_b32_e32 v204, v122
	v_mov_b32_e32 v205, v126
	s_nop 3
	ds_read_b128 v[208:211], v143
	s_waitcnt lgkmcnt(1)
	s_barrier
	ds_read_b128 v[212:215], v144
	ds_read_b128 v[216:219], v145
	s_waitcnt lgkmcnt(2)
	v_smfmac_f32_16x16x64_f16 v[200:203], v[208:211], v[42:49], v191
	ds_read_b128 v[220:223], v146
	v_smfmac_f32_16x16x64_f16 v[204:207], v[208:211], v[74:81], v191
	s_waitcnt lgkmcnt(2)
	v_smfmac_f32_16x16x64_f16 v[200:203], v[212:215], v[50:57], v191
	v_smfmac_f32_16x16x64_f16 v[204:207], v[212:215], v[82:89], v191
	s_waitcnt lgkmcnt(1)
	v_smfmac_f32_16x16x64_f16 v[200:203], v[216:219], v[58:65], v191
	v_smfmac_f32_16x16x64_f16 v[204:207], v[216:219], v[90:97], v191
	s_waitcnt lgkmcnt(0)
	v_smfmac_f32_16x16x64_f16 v[200:203], v[220:223], v[66:73], v191
	v_smfmac_f32_16x16x64_f16 v[204:207], v[220:223], v[98:105], v191
	s_nop 6
	v_cndmask_b32_e64 v172, v201, v200, s[6:7]
	v_cndmask_b32_e64 v172, v172, v204, s[0:1]
	v_cndmask_b32_e64 v172, v172, v205, s[4:5]
	v_exp_f32_e32 v172, v172
	s_nop 0
	v_add_f32_e32 v172, 1.0, v172
	v_rcp_f32_e32 v172, v172
	s_nop 0
	v_fmac_f32_e32 v137, v172, v136
	s_nop 1
	v_add_f32_dpp v136, v137, v137 quad_perm:[1,0,3,2] row_mask:0xf bank_mask:0xf bound_ctrl:1
	s_nop 1
	v_add_f32_dpp v136, v136, v136 quad_perm:[2,3,0,1] row_mask:0xf bank_mask:0xf bound_ctrl:1
	s_nop 1
	v_add_f32_dpp v136, v136, v136 row_half_mirror row_mask:0xf bank_mask:0xf bound_ctrl:1
	v_cvt_f16_f32_e32 v137, v136
	ds_write_b16 v150, v137
	s_waitcnt lgkmcnt(0)
	s_barrier
	ds_read_b128 v[156:159], v147
	s_nop 3
	ds_read_b32 v137, v134 offset:160
	v_add_f32_e32 v135, v135, v136
	s_waitcnt lgkmcnt(1)
	v_smfmac_f32_16x16x64_f16 v[130:133], v[156:159], v[248:255], v191
	s_nop 7
	v_cndmask_b32_e64 v156, v130, v131, s[0:1]
	v_exp_f32_e64 v158, -|v156|
	v_max_f32 v159, 0, v156
	v_add_f32 v158, 1.0, v158
	v_log_f32 v158, v158
	s_nop 0
	v_fma_mixlo_f16 v157, v158, 1.0, v159
	ds_write_b16 v148, v157
	v_mov_b32_e32 v192, v106
	v_mov_b32_e32 v193, v110
	v_mul_f32 v136, -2.0, v137
	s_nop 6
	ds_read_b128 v[208:211], v139
	s_waitcnt lgkmcnt(1)
	s_barrier
	ds_read_b128 v[212:215], v140
	ds_read_b128 v[216:219], v141
	s_waitcnt lgkmcnt(2)
	v_smfmac_f32_16x16x64_f16 v[192:195], v[208:211], v[6:13], v191
	ds_read_b128 v[220:223], v142
	s_waitcnt lgkmcnt(2)
	v_smfmac_f32_16x16x64_f16 v[192:195], v[212:215], v[14:21], v191
	s_waitcnt lgkmcnt(1)
	v_smfmac_f32_16x16x64_f16 v[192:195], v[216:219], v[26:33], v191
	s_waitcnt lgkmcnt(0)
	v_smfmac_f32_16x16x64_f16 v[192:195], v[220:223], v[34:41], v191
	s_nop 7
	v_cndmask_b32_e64 v156, v192, v193, s[0:1]
	v_exp_f32_e64 v158, -|v156|
	v_max_f32 v159, 0, v156
	v_add_f32 v158, 1.0, v158
	v_log_f32 v158, v158
	s_nop 0
	v_fma_mixlo_f16 v157, v158, 1.0, v159
	ds_write_b16 v149, v157
	v_mov_b32_e32 v200, v114
	v_mov_b32_e32 v201, v118
	v_mov_b32_e32 v204, v122
	v_mov_b32_e32 v205, v126
	s_nop 3
	ds_read_b128 v[208:211], v143
	s_waitcnt lgkmcnt(1)
	s_barrier
	ds_read_b128 v[212:215], v144
	ds_read_b128 v[216:219], v145
	s_waitcnt lgkmcnt(2)
	v_smfmac_f32_16x16x64_f16 v[200:203], v[208:211], v[42:49], v191
	ds_read_b128 v[220:223], v146
	v_smfmac_f32_16x16x64_f16 v[204:207], v[208:211], v[74:81], v191
	s_waitcnt lgkmcnt(2)
	v_smfmac_f32_16x16x64_f16 v[200:203], v[212:215], v[50:57], v191
	v_smfmac_f32_16x16x64_f16 v[204:207], v[212:215], v[82:89], v191
	s_waitcnt lgkmcnt(1)
	v_smfmac_f32_16x16x64_f16 v[200:203], v[216:219], v[58:65], v191
	v_smfmac_f32_16x16x64_f16 v[204:207], v[216:219], v[90:97], v191
	s_waitcnt lgkmcnt(0)
	v_smfmac_f32_16x16x64_f16 v[200:203], v[220:223], v[66:73], v191
	v_smfmac_f32_16x16x64_f16 v[204:207], v[220:223], v[98:105], v191
	s_nop 6
	v_cndmask_b32_e64 v172, v201, v200, s[6:7]
	v_cndmask_b32_e64 v172, v172, v204, s[0:1]
	v_cndmask_b32_e64 v172, v172, v205, s[4:5]
	v_exp_f32_e32 v172, v172
	s_nop 0
	v_add_f32_e32 v172, 1.0, v172
	v_rcp_f32_e32 v172, v172
	s_nop 0
	v_fmac_f32_e32 v137, v172, v136
	s_nop 1
	v_add_f32_dpp v136, v137, v137 quad_perm:[1,0,3,2] row_mask:0xf bank_mask:0xf bound_ctrl:1
	s_nop 1
	v_add_f32_dpp v136, v136, v136 quad_perm:[2,3,0,1] row_mask:0xf bank_mask:0xf bound_ctrl:1
	s_nop 1
	v_add_f32_dpp v136, v136, v136 row_half_mirror row_mask:0xf bank_mask:0xf bound_ctrl:1
	v_cvt_f16_f32_e32 v137, v136
	ds_write_b16 v150, v137
	s_waitcnt lgkmcnt(0)
	s_barrier
	ds_read_b128 v[156:159], v147
	s_nop 3
	ds_read_b32 v137, v134 offset:192
	v_add_f32_e32 v135, v135, v136
	s_waitcnt lgkmcnt(1)
	v_smfmac_f32_16x16x64_f16 v[130:133], v[156:159], v[248:255], v191
	s_nop 7
	v_cndmask_b32_e64 v152, v130, v131, s[0:1]
	v_exp_f32_e64 v158, -|v152|
	v_max_f32 v159, 0, v152
	v_add_f32 v158, 1.0, v158
	v_log_f32 v158, v158
	s_nop 0
	v_fma_mixlo_f16 v153, v158, 1.0, v159
	ds_write_b16 v148, v153
	v_mov_b32_e32 v192, v106
	v_mov_b32_e32 v193, v110
	v_mul_f32 v136, -2.0, v137
	s_nop 6
	ds_read_b128 v[208:211], v139
	s_waitcnt lgkmcnt(1)
	s_barrier
	ds_read_b128 v[212:215], v140
	ds_read_b128 v[216:219], v141
	s_waitcnt lgkmcnt(2)
	v_smfmac_f32_16x16x64_f16 v[192:195], v[208:211], v[6:13], v191
	ds_read_b128 v[220:223], v142
	s_waitcnt lgkmcnt(2)
	v_smfmac_f32_16x16x64_f16 v[192:195], v[212:215], v[14:21], v191
	s_waitcnt lgkmcnt(1)
	v_smfmac_f32_16x16x64_f16 v[192:195], v[216:219], v[26:33], v191
	s_waitcnt lgkmcnt(0)
	v_smfmac_f32_16x16x64_f16 v[192:195], v[220:223], v[34:41], v191
	s_nop 7
	v_cndmask_b32_e64 v152, v192, v193, s[0:1]
	v_exp_f32_e64 v158, -|v152|
	v_max_f32 v159, 0, v152
	v_add_f32 v158, 1.0, v158
	v_log_f32 v158, v158
	s_nop 0
	v_fma_mixlo_f16 v153, v158, 1.0, v159
	ds_write_b16 v149, v153
	v_mov_b32_e32 v200, v114
	v_mov_b32_e32 v201, v118
	v_mov_b32_e32 v204, v122
	v_mov_b32_e32 v205, v126
	s_nop 3
	ds_read_b128 v[208:211], v143
	s_waitcnt lgkmcnt(1)
	s_barrier
	ds_read_b128 v[212:215], v144
	ds_read_b128 v[216:219], v145
	s_waitcnt lgkmcnt(2)
	v_smfmac_f32_16x16x64_f16 v[200:203], v[208:211], v[42:49], v191
	ds_read_b128 v[220:223], v146
	v_smfmac_f32_16x16x64_f16 v[204:207], v[208:211], v[74:81], v191
	s_waitcnt lgkmcnt(2)
	v_smfmac_f32_16x16x64_f16 v[200:203], v[212:215], v[50:57], v191
	v_smfmac_f32_16x16x64_f16 v[204:207], v[212:215], v[82:89], v191
	s_waitcnt lgkmcnt(1)
	v_smfmac_f32_16x16x64_f16 v[200:203], v[216:219], v[58:65], v191
	v_smfmac_f32_16x16x64_f16 v[204:207], v[216:219], v[90:97], v191
	s_waitcnt lgkmcnt(0)
	v_smfmac_f32_16x16x64_f16 v[200:203], v[220:223], v[66:73], v191
	v_smfmac_f32_16x16x64_f16 v[204:207], v[220:223], v[98:105], v191
	s_nop 6
	v_cndmask_b32_e64 v152, v201, v200, s[6:7]
	v_cndmask_b32_e64 v152, v152, v204, s[0:1]
	v_cndmask_b32_e64 v152, v152, v205, s[4:5]
	v_exp_f32_e32 v152, v152
	s_nop 0
	v_add_f32_e32 v152, 1.0, v152
	v_rcp_f32_e32 v152, v152
	s_nop 0
	v_fmac_f32_e32 v137, v152, v136
	s_nop 1
	v_add_f32_dpp v136, v137, v137 quad_perm:[1,0,3,2] row_mask:0xf bank_mask:0xf bound_ctrl:1
	s_nop 1
	v_add_f32_dpp v136, v136, v136 quad_perm:[2,3,0,1] row_mask:0xf bank_mask:0xf bound_ctrl:1
	s_nop 1
	v_add_f32_dpp v136, v136, v136 row_half_mirror row_mask:0xf bank_mask:0xf bound_ctrl:1
	v_cvt_f16_f32_e32 v137, v136
	ds_write_b16 v150, v137
	s_waitcnt lgkmcnt(0)
	s_barrier
	ds_read_b128 v[158:161], v147
	v_add_f32_e32 v152, v135, v136
	ds_read_b32 v153, v134 offset:224
	s_addk_i32 s3, 0x100
	s_cmpk_eq_u32 s3, 0xfa20
	s_waitcnt lgkmcnt(1)
	v_smfmac_f32_16x16x64_f16 v[130:133], v[158:161], v[248:255], v191
	s_nop 7
	v_cndmask_b32_e64 v154, v130, v131, s[0:1]
	s_cbranch_scc0 .LBB0_21
	s_and_saveexec_b64 s[0:1], vcc
	ds_write_b32 v1, v152
	s_or_b64 exec, exec, s[0:1]
	v_cmp_gt_u32_e32 vcc, 10, v0
	s_waitcnt lgkmcnt(0)
	s_barrier
	s_and_saveexec_b64 s[0:1], vcc
	s_cbranch_execz .LBB0_28
	v_lshlrev_b32_e32 v1, 2, v0
	global_load_dword v1, v1, s[12:13]
	v_mov_b32_e32 v139, 0
	v_lshl_add_u64 v[2:3], s[10:11], 0, v[138:139]
	v_lshl_add_u64 v[2:3], v[2:3], 0, 28
	s_mov_b32 s0, 0
